# code layout: never-taken oversize-tile paths moved out of line behind s_endpgm so the hot path of both layer kernels is straight-line
# speedup vs baseline: 1.0067x; 1.0013x over previous
.LBB4_36:
	s_or_b64 exec, exec, s[0:1]
	s_waitcnt lgkmcnt(1)
	v_subrev_u32_e32 v1, s20, v1
	s_movk_i32 s0, 0x400
	v_cmp_lt_i32_e64 s[0:1], s0, v1
	v_mov_b32_e32 v27, v10
	v_lshl_add_u64 v[22:23], s[24:25], 0, v[26:27]
	v_lshl_add_u64 v[24:25], s[4:5], 0, v[26:27]
	v_lshl_add_u64 v[28:29], s[6:7], 0, v[26:27]
	s_and_b64 vcc, exec, s[0:1]
	s_waitcnt lgkmcnt(0)
	v_cmp_lt_i32_e64 s[2:3], v32, v33
	s_cbranch_vccnz .Lover4

.Ll0_p2_done:
	v_mov_b32_e32 v1, v17
	v_mov_b64_e32 v[16:17], v[8:9]
	v_mov_b64_e32 v[14:15], v[6:7]
	v_mov_b64_e32 v[12:13], v[4:5]
	v_mov_b64_e32 v[10:11], v[2:3]
.LBB4_70:
	v_lshlrev_b32_e32 v2, 4, v0
	global_load_dwordx4 v[6:9], v2, s[18:19]
	v_mov_b32_e32 v3, 0
	v_lshl_add_u64 v[22:23], s[18:19], 0, v[2:3]
	v_add_co_u32_e32 v2, vcc, 0x2000, v22
	v_cvt_pk_f16_f32 v17, v16, v17
	s_nop 0
	v_addc_co_u32_e32 v3, vcc, 0, v23, vcc
	s_waitcnt lgkmcnt(0)
	global_load_dwordx4 v[18:21], v[2:3], off
	v_add_co_u32_e32 v2, vcc, 0x4000, v22
	v_cvt_pk_f16_f32 v16, v14, v15
	s_nop 0
	v_addc_co_u32_e32 v3, vcc, 0, v23, vcc
	global_load_dwordx4 v[2:5], v[2:3], off
	v_cvt_pk_f16_f32 v14, v10, v11
	s_movk_i32 s2, 0x110
	v_add_co_u32_e32 v10, vcc, 0x6000, v22
	v_cvt_pk_f16_f32 v15, v12, v13
	v_mad_u32_u24 v1, v1, s2, v26
	v_addc_co_u32_e32 v11, vcc, 0, v23, vcc
	ds_write_b128 v1, v[14:17]
	global_load_dwordx4 v[14:17], v[10:11], off
	v_and_b32_e32 v27, 48, v0
	v_mad_u32_u24 v40, v42, s2, v27
	s_waitcnt lgkmcnt(0)
	s_barrier
	ds_read_b128 v[10:13], v40
	ds_read_b128 v[22:25], v40 offset:64
	ds_read_b128 v[28:31], v40 offset:4352
	ds_read_b128 v[32:35], v40 offset:4416
	ds_read_b128 v[36:39], v40 offset:8704
	ds_read_b128 v[44:47], v40 offset:8768
	ds_read_b128 v[48:51], v40 offset:13056
	ds_read_b128 v[52:55], v40 offset:13120
	v_mbcnt_hi_u32_b32 v1, -1, v43
	s_waitcnt vmcnt(3) lgkmcnt(7)
	v_mfma_f32_16x16x32_f16 v[10:13], v[10:13], v[6:9], 0
	s_waitcnt lgkmcnt(5)
	v_mfma_f32_16x16x32_f16 v[28:31], v[28:31], v[6:9], 0
	s_waitcnt lgkmcnt(3)
	v_mfma_f32_16x16x32_f16 v[36:39], v[36:39], v[6:9], 0
	s_waitcnt lgkmcnt(1)
	v_mfma_f32_16x16x32_f16 v[6:9], v[48:51], v[6:9], 0
	s_waitcnt vmcnt(2)
	v_mfma_f32_16x16x32_f16 v[10:13], v[22:25], v[18:21], v[10:13]
	v_mfma_f32_16x16x32_f16 v[22:25], v[32:35], v[18:21], v[28:31]
	v_mfma_f32_16x16x32_f16 v[28:31], v[44:47], v[18:21], v[36:39]
	s_waitcnt lgkmcnt(0)
	v_mfma_f32_16x16x32_f16 v[6:9], v[52:55], v[18:21], v[6:9]
	ds_read_b128 v[18:21], v40 offset:128
	ds_read_b128 v[32:35], v40 offset:192
	s_waitcnt vmcnt(1) lgkmcnt(1)
	v_mfma_f32_16x16x32_f16 v[10:13], v[18:21], v[2:5], v[10:13]
	ds_read_b128 v[18:21], v40 offset:4480
	ds_read_b128 v[36:39], v40 offset:4544
	s_waitcnt lgkmcnt(1)
	v_mfma_f32_16x16x32_f16 v[44:47], v[18:21], v[2:5], v[22:25]
	ds_read_b128 v[18:21], v40 offset:8832
	ds_read_b128 v[48:51], v40 offset:8896
	s_waitcnt lgkmcnt(1)
	v_mfma_f32_16x16x32_f16 v[28:31], v[18:21], v[2:5], v[28:31]
	ds_read_b128 v[22:25], v40 offset:13184
	ds_read_b128 v[18:21], v40 offset:13248
	s_waitcnt lgkmcnt(1)
	v_mfma_f32_16x16x32_f16 v[22:25], v[22:25], v[2:5], v[6:9]
	v_and_b32_e32 v2, 64, v1
	s_waitcnt vmcnt(0)
	v_mfma_f32_16x16x32_f16 v[10:13], v[32:35], v[14:17], v[10:13]
	v_add_u32_e32 v34, 64, v2
	v_xor_b32_e32 v32, 16, v1
	v_cmp_lt_i32_e32 vcc, v32, v34
	v_mfma_f32_16x16x32_f16 v[6:9], v[36:39], v[14:17], v[44:47]
	v_xor_b32_e32 v33, 32, v1
	v_mfma_f32_16x16x32_f16 v[2:5], v[48:51], v[14:17], v[28:31]
	s_waitcnt lgkmcnt(0)
	v_mfma_f32_16x16x32_f16 v[14:17], v[18:21], v[14:17], v[22:25]
	v_add_f32_e32 v18, 0, v10
	v_mul_f32_e32 v19, v11, v11
	v_add_f32_e32 v18, v18, v11
	v_fmac_f32_e32 v19, v10, v10
	v_add_f32_e32 v18, v18, v12
	v_fmac_f32_e32 v19, v12, v12
	v_add_f32_e32 v18, v18, v13
	v_fmac_f32_e32 v19, v13, v13
	v_add_f32_e32 v18, v18, v6
	v_fmac_f32_e32 v19, v6, v6
	v_add_f32_e32 v18, v18, v7
	v_fmac_f32_e32 v19, v7, v7
	v_add_f32_e32 v18, v18, v8
	v_fmac_f32_e32 v19, v8, v8
	v_add_f32_e32 v18, v18, v9
	v_fmac_f32_e32 v19, v9, v9
	v_add_f32_e32 v18, v18, v2
	v_fmac_f32_e32 v19, v2, v2
	v_add_f32_e32 v18, v18, v3
	v_fmac_f32_e32 v19, v3, v3
	v_add_f32_e32 v18, v18, v4
	v_fmac_f32_e32 v19, v4, v4
	v_add_f32_e32 v18, v18, v5
	v_fmac_f32_e32 v19, v5, v5
	v_add_f32_e32 v18, v18, v14
	v_fmac_f32_e32 v19, v14, v14
	v_add_f32_e32 v18, v18, v15
	v_fmac_f32_e32 v19, v15, v15
	v_cndmask_b32_e32 v28, v1, v32, vcc
	v_add_f32_e32 v18, v18, v16
	v_fmac_f32_e32 v19, v16, v16
	v_lshlrev_b32_e32 v28, 2, v28
	v_add_f32_e32 v18, v18, v17
	v_fmac_f32_e32 v19, v17, v17
	ds_bpermute_b32 v20, v28, v18
	ds_bpermute_b32 v21, v28, v19
	v_cmp_lt_i32_e32 vcc, v33, v34
	s_waitcnt lgkmcnt(1)
	v_add_f32_e32 v18, v18, v20
	v_cndmask_b32_e32 v1, v1, v33, vcc
	v_lshlrev_b32_e32 v1, 2, v1
	s_waitcnt lgkmcnt(0)
	v_add_f32_e32 v19, v19, v21
	ds_bpermute_b32 v20, v1, v18
	ds_bpermute_b32 v21, v1, v19
	v_lshrrev_b32_e32 v1, 6, v0
	v_cmp_eq_u32_e32 vcc, 0, v27
	s_and_saveexec_b64 s[0:1], vcc
	s_cbranch_execz .LBB4_72
	s_lshr_b32 s3, s15, 29
	s_add_i32 s3, s14, s3
	s_and_b32 s3, s3, 0xfffff8
	s_sub_i32 s3, s14, s3
	s_lshl_b32 s4, s3, 8
	s_ashr_i32 s5, s4, 31
	s_lshl_b64 s[4:5], s[4:5], 2
	s_add_u32 s4, s16, s4
	v_lshlrev_b32_e32 v22, 2, v42
	s_addc_u32 s5, s17, s5
	v_lshl_or_b32 v22, v1, 6, v22
	s_waitcnt lgkmcnt(1)
	v_add_f32_e32 v18, v18, v20
	s_waitcnt lgkmcnt(0)
	v_add_f32_e32 v19, v19, v21
	global_atomic_add_f32 v22, v18, s[4:5]
	global_atomic_add_f32 v22, v19, s[4:5] offset:512

.Lover4:
	v_mov_b64_e32 v[16:17], v[8:9]
	v_mov_b64_e32 v[14:15], v[6:7]
	v_mov_b64_e32 v[12:13], v[4:5]
	v_mov_b64_e32 v[10:11], v[2:3]
	s_and_saveexec_b64 s[4:5], s[2:3]
	s_cbranch_execz .LBB4_44
	v_ashrrev_i32_e32 v11, 31, v32
	v_mov_b32_e32 v10, v32
	v_lshlrev_b64 v[12:13], 2, v[10:11]
	v_lshlrev_b64 v[10:11], 8, v[10:11]
	v_lshl_add_u64 v[38:39], v[28:29], 0, v[10:11]
	v_add_u32_e32 v10, 1, v32
	v_ashrrev_i32_e32 v11, 31, v10
	v_lshlrev_b64 v[10:11], 8, v[10:11]
	v_lshl_add_u64 v[34:35], s[22:23], 0, v[12:13]
	v_lshl_add_u64 v[36:37], s[10:11], 0, v[12:13]
	v_lshl_add_u64 v[40:41], v[28:29], 0, v[10:11]
	v_mov_b64_e32 v[16:17], v[8:9]
	s_mov_b64 s[2:3], 0
	s_mov_b64 s[6:7], 0x200
	v_mov_b64_e32 v[14:15], v[6:7]
	v_mov_b64_e32 v[12:13], v[4:5]
	v_mov_b64_e32 v[10:11], v[2:3]
	v_mov_b32_e32 v1, v32
	s_branch .LBB4_40

.LBB4_40:
	global_load_dword v18, v[34:35], off
	global_load_dword v20, v[36:37], off
	v_add_u32_e32 v27, 1, v1
	v_cmp_lt_i32_e32 vcc, v27, v33
	s_waitcnt vmcnt(1)
	v_ashrrev_i32_e32 v19, 31, v18
	v_lshlrev_b64 v[18:19], 9, v[18:19]
	v_lshl_add_u64 v[18:19], v[24:25], 0, v[18:19]
	global_load_dwordx4 v[46:49], v[18:19], off offset:256 nt
	global_load_dwordx4 v[50:53], v[18:19], off nt
	s_waitcnt vmcnt(2)
	v_ashrrev_i32_e32 v21, 31, v20
	v_lshlrev_b64 v[18:19], 8, v[20:21]
	v_lshl_add_u64 v[18:19], v[22:23], 0, v[18:19]
	global_load_dwordx4 v[18:21], v[18:19], off
	s_waitcnt vmcnt(2)
	v_cvt_f16_f32_e32 v45, v49
	v_cvt_f16_f32_e32 v54, v48
	v_cvt_f16_f32_e32 v55, v47
	v_cvt_f16_f32_e32 v56, v46
	s_waitcnt vmcnt(1)
	v_cvt_f16_f32_e32 v57, v53
	v_cvt_f16_f32_e32 v58, v52
	v_cvt_f16_f32_e32 v59, v51
	v_cvt_f16_f32_e32 v60, v50
	v_cvt_pk_f16_f32 v49, v48, v49
	v_cvt_pk_f16_f32 v48, v46, v47
	v_cvt_pk_f16_f32 v47, v52, v53
	v_cvt_pk_f16_f32 v46, v50, v51
	s_waitcnt vmcnt(0)
	v_cvt_f32_f16_e32 v50, v18
	v_cvt_f32_f16_sdwa v18, v18 dst_sel:DWORD dst_unused:UNUSED_PAD src0_sel:WORD_1
	v_cvt_f32_f16_e32 v51, v19
	v_cvt_f32_f16_sdwa v19, v19 dst_sel:DWORD dst_unused:UNUSED_PAD src0_sel:WORD_1
	v_cvt_f32_f16_e32 v52, v20
	v_cvt_f32_f16_sdwa v20, v20 dst_sel:DWORD dst_unused:UNUSED_PAD src0_sel:WORD_1
	v_cvt_f32_f16_e32 v53, v21
	v_cvt_f32_f16_sdwa v21, v21 dst_sel:DWORD dst_unused:UNUSED_PAD src0_sel:WORD_1
	global_store_dwordx4 v[38:39], v[46:49], off sc1
	s_nop 1
	v_cvt_f32_f16_e32 v46, v60
	v_cvt_f32_f16_e32 v47, v59
	v_cvt_f32_f16_e32 v48, v58
	v_cvt_f32_f16_e32 v49, v57
	v_cvt_f32_f16_e32 v56, v56
	v_cvt_f32_f16_e32 v55, v55
	v_cvt_f32_f16_e32 v54, v54
	v_cvt_f32_f16_e32 v45, v45
	v_add_f32_e32 v46, v46, v50
	v_add_f32_e32 v47, v18, v47
	v_add_f32_e32 v48, v51, v48
	v_add_f32_e32 v49, v19, v49
	v_add_f32_e32 v50, v52, v56
	v_add_f32_e32 v51, v20, v55
	v_add_f32_e32 v52, v53, v54
	v_add_f32_e32 v45, v21, v45
	v_max_f32_e32 v18, 0, v46
	v_max_f32_e32 v19, 0, v47
	v_max_f32_e32 v20, 0, v48
	v_max_f32_e32 v21, 0, v49
	v_max_f32_e32 v46, 0, v50
	v_max_f32_e32 v47, 0, v51
	v_max_f32_e32 v48, 0, v52
	v_max_f32_e32 v49, 0, v45
	v_pk_add_f32 v[10:11], v[10:11], v[18:19]
	v_pk_add_f32 v[12:13], v[12:13], v[20:21]
	v_pk_add_f32 v[14:15], v[14:15], v[46:47]
	v_pk_add_f32 v[16:17], v[16:17], v[48:49]
	s_and_saveexec_b64 s[8:9], vcc
	s_cbranch_execz .LBB4_39
	v_cndmask_b32_e32 v18, v1, v27, vcc
	v_ashrrev_i32_e32 v19, 31, v18
	v_lshlrev_b64 v[18:19], 2, v[18:19]
	v_lshl_add_u64 v[20:21], s[22:23], 0, v[18:19]
	global_load_dword v20, v[20:21], off
	v_lshl_add_u64 v[18:19], s[10:11], 0, v[18:19]
	global_load_dword v50, v[18:19], off
	s_waitcnt vmcnt(1)
	v_ashrrev_i32_e32 v21, 31, v20
	v_lshlrev_b64 v[18:19], 9, v[20:21]
	v_lshl_add_u64 v[46:47], v[24:25], 0, v[18:19]
	global_load_dwordx4 v[18:21], v[46:47], off offset:256 nt
	s_nop 0
	global_load_dwordx4 v[46:49], v[46:47], off nt
	s_waitcnt vmcnt(2)
	v_ashrrev_i32_e32 v51, 31, v50
	v_lshlrev_b64 v[50:51], 8, v[50:51]
	v_lshl_add_u64 v[50:51], v[22:23], 0, v[50:51]
	global_load_dwordx4 v[50:53], v[50:51], off
	s_waitcnt vmcnt(2)
	v_cvt_f16_f32_e32 v27, v21
	v_cvt_f16_f32_e32 v45, v20
	v_cvt_f16_f32_e32 v54, v19
	v_cvt_f16_f32_e32 v55, v18
	s_waitcnt vmcnt(1)
	v_cvt_f16_f32_e32 v56, v49
	v_cvt_f16_f32_e32 v57, v48
	v_cvt_f16_f32_e32 v58, v47
	v_cvt_f16_f32_e32 v59, v46
	v_cvt_pk_f16_f32 v21, v20, v21
	v_cvt_pk_f16_f32 v20, v18, v19
	v_cvt_pk_f16_f32 v19, v48, v49
	v_cvt_pk_f16_f32 v18, v46, v47
	s_waitcnt vmcnt(0)
	v_cvt_f32_f16_e32 v46, v50
	v_cvt_f32_f16_sdwa v47, v50 dst_sel:DWORD dst_unused:UNUSED_PAD src0_sel:WORD_1
	v_cvt_f32_f16_e32 v48, v51
	v_cvt_f32_f16_sdwa v49, v51 dst_sel:DWORD dst_unused:UNUSED_PAD src0_sel:WORD_1
	v_cvt_f32_f16_e32 v50, v52
	v_cvt_f32_f16_sdwa v51, v52 dst_sel:DWORD dst_unused:UNUSED_PAD src0_sel:WORD_1
	v_cvt_f32_f16_e32 v52, v53
	v_cvt_f32_f16_sdwa v53, v53 dst_sel:DWORD dst_unused:UNUSED_PAD src0_sel:WORD_1
	global_store_dwordx4 v[40:41], v[18:21], off sc1
	s_nop 1
	v_cvt_f32_f16_e32 v18, v59
	v_cvt_f32_f16_e32 v19, v58
	v_cvt_f32_f16_e32 v20, v57
	v_cvt_f32_f16_e32 v21, v56
	v_cvt_f32_f16_e32 v55, v55
	v_cvt_f32_f16_e32 v54, v54
	v_cvt_f32_f16_e32 v45, v45
	v_cvt_f32_f16_e32 v27, v27
	v_add_f32_e32 v18, v46, v18
	v_add_f32_e32 v19, v47, v19
	v_add_f32_e32 v20, v48, v20
	v_add_f32_e32 v21, v49, v21
	v_add_f32_e32 v46, v50, v55
	v_add_f32_e32 v47, v51, v54
	v_add_f32_e32 v45, v52, v45
	v_add_f32_e32 v27, v53, v27
	v_max_f32_e32 v18, 0, v18
	v_max_f32_e32 v19, 0, v19
	v_max_f32_e32 v20, 0, v20
	v_max_f32_e32 v21, 0, v21
	v_max_f32_e32 v46, 0, v46
	v_max_f32_e32 v47, 0, v47
	v_max_f32_e32 v48, 0, v45
	v_max_f32_e32 v49, 0, v27
	v_pk_add_f32 v[10:11], v[18:19], v[10:11]
	v_pk_add_f32 v[12:13], v[20:21], v[12:13]
	v_pk_add_f32 v[14:15], v[46:47], v[14:15]
	v_pk_add_f32 v[16:17], v[48:49], v[16:17]
	s_branch .LBB4_39
.LBB4_43:
	s_or_b64 exec, exec, s[2:3]
.LBB4_44:
	s_or_b64 exec, exec, s[4:5]
	s_cbranch_execnz .LBB4_52
.LBB4_52:
	s_movk_i32 s2, 0x110
	v_cvt_pk_f16_f32 v5, v16, v17
	v_cvt_pk_f16_f32 v4, v14, v15
	v_cvt_pk_f16_f32 v3, v12, v13
	v_cvt_pk_f16_f32 v2, v10, v11
	v_mad_u32_u24 v1, v44, s2, v26
	ds_write_b128 v1, v[2:5]
	v_or_b32_e32 v1, 1, v31
	v_mov_b32_e32 v2, 0x6400
	v_lshl_or_b32 v2, v1, 2, v2
	ds_read2_b32 v[32:33], v2 offset1:1
	v_add_u32_e32 v10, s30, v1
	s_mov_b32 s2, 0x186a0
	v_mov_b32_e32 v2, 0
	v_cmp_gt_i32_e32 vcc, s2, v10
	v_mov_b32_e32 v3, v2
	v_mov_b32_e32 v4, v2
	v_mov_b32_e32 v5, v2
	v_mov_b32_e32 v6, v2
	v_mov_b32_e32 v7, v2
	v_mov_b32_e32 v8, v2
	v_mov_b32_e32 v9, v2
	s_and_saveexec_b64 s[2:3], vcc
	s_cbranch_execz .LBB4_54
	v_ashrrev_i32_e32 v11, 31, v10
	v_lshlrev_b64 v[2:3], 8, v[10:11]
	v_lshl_add_u64 v[2:3], v[22:23], 0, v[2:3]
	global_load_dwordx4 v[2:5], v[2:3], off
	s_waitcnt vmcnt(0)
	v_cvt_f32_f16_e32 v10, v2
	v_cvt_f32_f16_e32 v12, v3
	v_cvt_f32_f16_e32 v6, v4
	v_cvt_f32_f16_e32 v8, v5
	v_cvt_f32_f16_sdwa v9, v5 dst_sel:DWORD dst_unused:UNUSED_PAD src0_sel:WORD_1
	v_cvt_f32_f16_sdwa v7, v4 dst_sel:DWORD dst_unused:UNUSED_PAD src0_sel:WORD_1
	v_cvt_f32_f16_sdwa v13, v3 dst_sel:DWORD dst_unused:UNUSED_PAD src0_sel:WORD_1
	v_cvt_f32_f16_sdwa v11, v2 dst_sel:DWORD dst_unused:UNUSED_PAD src0_sel:WORD_1
	v_pk_mul_f32 v[8:9], v[30:31], v[8:9] op_sel_hi:[0,1]
	v_pk_mul_f32 v[6:7], v[30:31], v[6:7] op_sel_hi:[0,1]
	v_pk_mul_f32 v[4:5], v[30:31], v[12:13] op_sel_hi:[0,1]
	v_pk_mul_f32 v[2:3], v[30:31], v[10:11] op_sel_hi:[0,1]

.LBB4_62:
	s_or_b64 exec, exec, s[2:3]
	s_branch .LBB4_70

.LBB5_11:
	s_or_b64 exec, exec, s[0:1]
	s_waitcnt vmcnt(0) lgkmcnt(1)
	v_sub_u32_e32 v2, v6, v28
	s_movk_i32 s0, 0x400
	v_cmp_lt_i32_e64 s[0:1], s0, v2
	v_lshl_add_u64 v[30:31], s[4:5], 0, v[26:27]
	v_lshl_add_u64 v[32:33], s[12:13], 0, v[26:27]
	s_and_b64 vcc, exec, s[0:1]
	s_waitcnt lgkmcnt(0)
	v_cmp_lt_i32_e64 s[2:3], v44, v45
	s_cbranch_vccnz .Lover5

.Ll1_p2_done:
	v_or_b32_e32 v27, 1, v35
	v_mov_b32_e32 v34, v42
	v_mov_b32_e32 v35, v43
	v_mov_b32_e32 v46, v40
	v_mov_b32_e32 v47, v41
	v_mov_b32_e32 v48, v38
	v_mov_b32_e32 v49, v39
	v_mov_b32_e32 v50, v36
	v_mov_b32_e32 v51, v37
.LBB5_61:
	v_and_b32_e32 v21, 63, v0
	v_lshrrev_b32_e32 v20, 5, v0
	v_and_b32_e32 v19, 6, v20
	s_waitcnt vmcnt(2)
	v_lshlrev_b32_e32 v2, 4, v21
	v_or_b32_e32 v18, 1, v20
	s_waitcnt vmcnt(1)
	v_lshl_or_b32 v14, v19, 10, v2
	v_lshl_or_b32 v2, v18, 10, v2
	global_load_dwordx4 v[22:25], v14, s[10:11]
	global_load_dwordx4 v[28:31], v2, s[10:11]
	v_or_b32_e32 v2, 0x2000, v14
	global_load_dwordx4 v[36:39], v2, s[10:11]
	v_or_b32_e32 v2, 0x2400, v14
	global_load_dwordx4 v[40:43], v2, s[10:11]
	v_or_b32_e32 v2, 0x4000, v14
	global_load_dwordx4 v[10:13], v2, s[10:11]
	v_or_b32_e32 v2, 0x4400, v14
	global_load_dwordx4 v[6:9], v2, s[10:11]
	v_or_b32_e32 v2, 0x6000, v14
	global_load_dwordx4 v[2:5], v2, s[10:11]
	v_or_b32_e32 v14, 0x6400, v14
	global_load_dwordx4 v[14:17], v14, s[10:11]
	s_movk_i32 s0, 0x110
	v_and_b32_e32 v32, 48, v0
	v_cvt_pk_f16_f32 v51, v50, v51
	v_cvt_pk_f16_f32 v50, v48, v49
	v_cvt_pk_f16_f32 v49, v46, v47
	v_cvt_pk_f16_f32 v48, v34, v35
	v_mad_u32_u24 v27, v27, s0, v26
	v_mad_u32_u24 v60, v1, s0, v32
	ds_write_b128 v27, v[48:51]
	s_waitcnt lgkmcnt(0)
	s_barrier
	ds_read_b128 v[32:35], v60
	ds_read_b128 v[44:47], v60 offset:64
	ds_read_b128 v[52:55], v60 offset:4352
	ds_read_b128 v[56:59], v60 offset:4416
	v_mbcnt_lo_u32_b32 v27, -1, 0
	v_mbcnt_hi_u32_b32 v27, -1, v27
	s_ashr_i32 s0, s25, 31
	s_lshr_b32 s0, s0, 29
	s_add_i32 s0, s25, s0
	s_and_b32 s0, s0, 0xfffff8
	s_sub_i32 s0, s25, s0
	s_lshl_b32 s0, s0, 8
	s_ashr_i32 s1, s0, 31
	s_lshl_b64 s[0:1], s[0:1], 2
	s_add_u32 s0, s8, s0
	s_addc_u32 s1, s9, s1
	s_waitcnt vmcnt(7) lgkmcnt(3)
	v_mfma_f32_16x16x32_f16 v[48:51], v[32:35], v[22:25], 0
	s_waitcnt vmcnt(6)
	v_mfma_f32_16x16x32_f16 v[32:35], v[32:35], v[28:31], 0
	s_waitcnt lgkmcnt(1)
	v_mfma_f32_16x16x32_f16 v[22:25], v[52:55], v[22:25], 0
	v_mfma_f32_16x16x32_f16 v[28:31], v[52:55], v[28:31], 0
	s_waitcnt vmcnt(5)
	v_mfma_f32_16x16x32_f16 v[48:51], v[44:47], v[36:39], v[48:51]
	s_waitcnt vmcnt(4)
	v_mfma_f32_16x16x32_f16 v[32:35], v[44:47], v[40:43], v[32:35]
	s_waitcnt lgkmcnt(0)
	v_mfma_f32_16x16x32_f16 v[22:25], v[56:59], v[36:39], v[22:25]
	v_mfma_f32_16x16x32_f16 v[28:31], v[56:59], v[40:43], v[28:31]
	ds_read_b128 v[36:39], v60 offset:128
	ds_read_b128 v[40:43], v60 offset:4480
	ds_read_b128 v[44:47], v60 offset:192
	s_waitcnt vmcnt(3) lgkmcnt(2)
	v_mfma_f32_16x16x32_f16 v[48:51], v[36:39], v[10:13], v[48:51]
	s_waitcnt vmcnt(2)
	v_mfma_f32_16x16x32_f16 v[32:35], v[36:39], v[6:9], v[32:35]
	ds_read_b128 v[36:39], v60 offset:4544
	s_waitcnt lgkmcnt(2)
	v_mfma_f32_16x16x32_f16 v[52:55], v[40:43], v[10:13], v[22:25]
	v_and_b32_e32 v10, 64, v27
	s_nop 1
	v_xor_b32_e32 v22, 16, v27
	v_mfma_f32_16x16x32_f16 v[28:31], v[40:43], v[6:9], v[28:31]
	v_add_u32_e32 v6, 64, v10
	v_xor_b32_e32 v23, 32, v27
	v_cmp_lt_i32_e32 vcc, v22, v6
	s_waitcnt vmcnt(1) lgkmcnt(1)
	v_mfma_f32_16x16x32_f16 v[10:13], v[44:47], v[2:5], v[48:51]
	v_cndmask_b32_e32 v22, v27, v22, vcc
	v_cmp_lt_i32_e32 vcc, v23, v6
	s_waitcnt lgkmcnt(0)
	v_mfma_f32_16x16x32_f16 v[2:5], v[36:39], v[2:5], v[52:55]
	v_cndmask_b32_e32 v24, v27, v23, vcc
	v_lshlrev_b32_e32 v23, 2, v22
	v_lshlrev_b32_e32 v22, 2, v24
	s_nop 0
	v_add_f32_e32 v24, 0, v10
	v_mul_f32_e32 v25, v11, v11
	v_add_f32_e32 v24, v24, v11
	v_fmac_f32_e32 v25, v10, v10
	v_add_f32_e32 v24, v24, v12
	v_fmac_f32_e32 v25, v12, v12
	v_add_f32_e32 v24, v24, v13
	v_fmac_f32_e32 v25, v13, v13
	v_add_f32_e32 v24, v24, v2
	v_fmac_f32_e32 v25, v2, v2
	v_add_f32_e32 v24, v24, v3
	v_fmac_f32_e32 v25, v3, v3
	v_add_f32_e32 v24, v24, v4
	v_fmac_f32_e32 v25, v4, v4
	v_add_f32_e32 v24, v24, v5
	v_fmac_f32_e32 v25, v5, v5
	s_waitcnt vmcnt(0)
	v_mfma_f32_16x16x32_f16 v[6:9], v[44:47], v[14:17], v[32:35]
	ds_bpermute_b32 v27, v23, v24
	v_cmp_gt_u32_e32 vcc, 16, v21
	v_lshlrev_b32_e32 v21, 2, v1
	ds_bpermute_b32 v32, v23, v25
	v_mfma_f32_16x16x32_f16 v[14:17], v[36:39], v[14:17], v[28:31]
	s_waitcnt lgkmcnt(1)
	v_add_f32_e32 v24, v24, v27
	ds_bpermute_b32 v27, v22, v24
	s_waitcnt lgkmcnt(1)
	v_add_f32_e32 v25, v25, v32
	ds_bpermute_b32 v28, v22, v25
	s_and_saveexec_b64 s[2:3], vcc
	s_cbranch_execz .LBB5_63
	s_waitcnt lgkmcnt(1)
	v_add_f32_e32 v24, v24, v27
	v_lshl_or_b32 v27, v19, 6, v21
	s_waitcnt lgkmcnt(0)
	v_add_f32_e32 v25, v25, v28
	global_atomic_add_f32 v27, v24, s[0:1]
	global_atomic_add_f32 v27, v25, s[0:1] offset:512

.Lover5:
	v_mov_b32_e32 v53, v37
	v_mov_b32_e32 v52, v36
	v_mov_b32_e32 v51, v39
	v_mov_b32_e32 v50, v38
	v_mov_b32_e32 v49, v41
	v_mov_b32_e32 v48, v40
	v_mov_b32_e32 v47, v43
	v_mov_b32_e32 v46, v42
	s_and_saveexec_b64 s[16:17], s[2:3]
	s_cbranch_execz .LBB5_23
	v_ashrrev_i32_e32 v3, 31, v44
	v_mov_b32_e32 v2, v44
	v_lshl_add_u64 v[4:5], v[2:3], 2, s[14:15]
	v_lshlrev_b64 v[2:3], 8, v[2:3]
	v_lshl_or_b32 v2, v1, 4, v2
	v_lshl_add_u64 v[54:55], v[4:5], 0, 4
	v_lshl_add_u64 v[56:57], s[12:13], 0, v[2:3]
	s_mov_b64 s[18:19], 0
	s_mov_b64 s[20:21], 0x400
	v_mov_b32_e32 v27, v44
	v_mov_b64_e32 v[46:47], v[42:43]
	v_mov_b64_e32 v[48:49], v[40:41]
	v_mov_b64_e32 v[50:51], v[38:39]
	v_mov_b64_e32 v[52:53], v[36:37]
	s_branch .LBB5_15

.LBB5_20:
	v_cvt_f32_f16_e32 v10, v2
	v_cvt_f32_f16_e32 v11, v6
	v_cvt_f32_f16_sdwa v2, v2 dst_sel:DWORD dst_unused:UNUSED_PAD src0_sel:WORD_1
	v_cvt_f32_f16_sdwa v6, v6 dst_sel:DWORD dst_unused:UNUSED_PAD src0_sel:WORD_1
	v_add_f32_e32 v10, v10, v11
	v_max_f32_e32 v10, 0, v10
	v_add_f32_e32 v2, v2, v6
	v_max_f32_e32 v11, 0, v2
	v_cvt_f32_f16_e32 v2, v3
	v_cvt_f32_f16_e32 v6, v7
	v_cvt_f32_f16_sdwa v3, v3 dst_sel:DWORD dst_unused:UNUSED_PAD src0_sel:WORD_1
	v_cvt_f32_f16_sdwa v7, v7 dst_sel:DWORD dst_unused:UNUSED_PAD src0_sel:WORD_1
	v_pk_add_f32 v[46:47], v[10:11], v[46:47]
	v_add_f32_e32 v2, v2, v6
	v_cvt_f32_f16_e32 v6, v4
	v_add_f32_e32 v3, v3, v7
	v_cvt_f32_f16_e32 v7, v8
	v_cvt_f32_f16_sdwa v4, v4 dst_sel:DWORD dst_unused:UNUSED_PAD src0_sel:WORD_1
	v_cvt_f32_f16_sdwa v8, v8 dst_sel:DWORD dst_unused:UNUSED_PAD src0_sel:WORD_1
	v_max_f32_e32 v2, 0, v2
	v_max_f32_e32 v3, 0, v3
	v_pk_add_f32 v[48:49], v[2:3], v[48:49]
	v_add_f32_e32 v2, v6, v7
	v_add_f32_e32 v3, v4, v8
	v_cvt_f32_f16_e32 v4, v5
	v_cvt_f32_f16_e32 v6, v9
	v_cvt_f32_f16_sdwa v5, v5 dst_sel:DWORD dst_unused:UNUSED_PAD src0_sel:WORD_1
	v_cvt_f32_f16_sdwa v7, v9 dst_sel:DWORD dst_unused:UNUSED_PAD src0_sel:WORD_1
	v_max_f32_e32 v2, 0, v2
	v_max_f32_e32 v3, 0, v3
	v_pk_add_f32 v[50:51], v[2:3], v[50:51]
	v_add_f32_e32 v2, v4, v6
	v_add_f32_e32 v3, v5, v7
	v_max_f32_e32 v2, 0, v2
	v_max_f32_e32 v3, 0, v3
	v_pk_add_f32 v[52:53], v[2:3], v[52:53]
	s_branch .LBB5_14
.LBB5_22:
	s_or_b64 exec, exec, s[18:19]
.LBB5_23:
	s_or_b64 exec, exec, s[16:17]
	s_cbranch_execnz .LBB5_35
.LBB5_35:
	s_movk_i32 s2, 0x110
	s_waitcnt vmcnt(2)
	v_cvt_pk_f16_f32 v5, v52, v53
	v_cvt_pk_f16_f32 v4, v50, v51
	v_cvt_pk_f16_f32 v3, v48, v49
	v_cvt_pk_f16_f32 v2, v46, v47
	s_waitcnt vmcnt(0)
	v_mad_u32_u24 v6, v60, s2, v26
	ds_write_b128 v6, v[2:5]
	v_or_b32_e32 v27, 1, v35
	v_mov_b32_e32 v3, 0x3200
	v_lshl_or_b32 v3, v27, 2, v3
	ds_read2_b32 v[40:41], v3 offset1:1
	v_add_u32_e32 v2, s24, v27
	s_mov_b32 s2, 0x186a0
	v_cmp_gt_i32_e32 vcc, s2, v2
	v_mov_b32_e32 v44, 0
	v_mov_b32_e32 v45, 0
	v_mov_b32_e32 v42, 0
	v_mov_b32_e32 v43, 0
	v_mov_b32_e32 v38, 0
	v_mov_b32_e32 v39, 0
	v_mov_b32_e32 v36, 0
	v_mov_b32_e32 v37, 0
	s_and_saveexec_b64 s[2:3], vcc
	s_cbranch_execz .LBB5_37
	v_ashrrev_i32_e32 v3, 31, v2
	v_lshlrev_b64 v[2:3], 8, v[2:3]
	v_lshl_add_u64 v[2:3], v[30:31], 0, v[2:3]
	global_load_dwordx4 v[2:5], v[2:3], off
	s_waitcnt vmcnt(0)
	v_cvt_f32_f16_e32 v6, v2
	v_cvt_f32_f16_e32 v8, v3
	v_cvt_f32_f16_e32 v10, v4
	v_cvt_f32_f16_e32 v12, v5
	v_cvt_f32_f16_sdwa v13, v5 dst_sel:DWORD dst_unused:UNUSED_PAD src0_sel:WORD_1
	v_cvt_f32_f16_sdwa v11, v4 dst_sel:DWORD dst_unused:UNUSED_PAD src0_sel:WORD_1
	v_cvt_f32_f16_sdwa v9, v3 dst_sel:DWORD dst_unused:UNUSED_PAD src0_sel:WORD_1
	v_cvt_f32_f16_sdwa v7, v2 dst_sel:DWORD dst_unused:UNUSED_PAD src0_sel:WORD_1
	v_pk_mul_f32 v[36:37], v[34:35], v[12:13] op_sel_hi:[0,1]
	v_pk_mul_f32 v[38:39], v[34:35], v[10:11] op_sel_hi:[0,1]
	v_pk_mul_f32 v[42:43], v[34:35], v[8:9] op_sel_hi:[0,1]
	v_pk_mul_f32 v[44:45], v[34:35], v[6:7] op_sel_hi:[0,1]

.LBB5_49:
	s_or_b64 exec, exec, s[4:5]
	s_branch .LBB5_61
